# same as the pipelined indexer loop version, with the compiler's carry-in pad kept where the early vmcnt(0) was dropped
# baseline (speedup 1.0000x reference)
; __device__ __forceinline__ void dsa2_unit(LAS unsigned char* lds, const bf16* PROJ, const bf16* KIDX, const bf16* KVN, bf16* OLAT, float* sbuf, int b, int t0, int tid) {
;     ...
;         { const int ntiles = (t0 >> 5) + 1, tpw = (ntiles + 7) >> 3, tile0 = wave * tpw; int tile1 = tile0 + tpw; tile1 = tile1 < ntiles ? tile1 : ntiles;
;           const int ahead = (r & 3) + 4 * ((r >> 3) & 1), atok = ((r >> 2) & 1) + 2 * (r >> 4);
;           const bf16* qpa = PROJ + (rowb + t0 + atok) * NP + PC_QIDX + ahead * 32 + 8 * h; const bf16* qpb = qpa + (size_t)4 * NP;
;           const bf16x8 A0a = *(const bf16x8*)qpa, A1a = *(const bf16x8*)(qpa + 16), A0b = *(const bf16x8*)qpb, A1b = *(const bf16x8*)(qpb + 16);
;           float wq[32];
; #pragma unroll
;           for (int gq = 0; gq < 4; ++gq) { const v4u w0 = *(const v4u*)(PROJ + (rowb + t0 + h + 2 * gq) * NP + PC_WIDX);
;               wq[8 * gq] = 0.5f * bflo(w0.x); wq[8 * gq + 1] = 0.5f * bfhi(w0.x); wq[8 * gq + 2] = 0.5f * bflo(w0.y); wq[8 * gq + 3] = 0.5f * bfhi(w0.y); wq[8 * gq + 4] = 0.5f * bflo(w0.z); wq[8 * gq + 5] = 0.5f * bfhi(w0.z); wq[8 * gq + 6] = 0.5f * bflo(w0.w); wq[8 * gq + 7] = 0.5f * bfhi(w0.w); }
;           v4u A0c = {0u, 0u, 0u, 0u}, A1c = {0u, 0u, 0u, 0u};
;           if (r < 8) { const bf16* qrow = PROJ + (rowb + t0 + (r >> 2) + 2 * (r & 3)) * NP; const v4u wv = *(const v4u*)(qrow + PC_WIDX);
;               const float wl_[8] = {bflo(wv.x), bfhi(wv.x), bflo(wv.y), bfhi(wv.y), bflo(wv.z), bfhi(wv.z), bflo(wv.w), bfhi(wv.w)};
;               float a0[8], a1[8];
; #pragma unroll
;               for (int j = 0; j < 8; ++j) { a0[j] = 0.f; a1[j] = 0.f; }
; #pragma unroll
;               for (int hd = 0; hd < 8; ++hd) { const v4u q0 = *(const v4u*)(qrow + PC_QIDX + hd * 32 + 8 * h), q1 = *(const v4u*)(qrow + PC_QIDX + hd * 32 + 16 + 8 * h); const float hw = 0.5f * wl_[hd];
;                   a0[0] += hw * bflo(q0.x); a0[1] += hw * bfhi(q0.x); a0[2] += hw * bflo(q0.y); a0[3] += hw * bfhi(q0.y); a0[4] += hw * bflo(q0.z); a0[5] += hw * bfhi(q0.z); a0[6] += hw * bflo(q0.w); a0[7] += hw * bfhi(q0.w);
;                   a1[0] += hw * bflo(q1.x); a1[1] += hw * bfhi(q1.x); a1[2] += hw * bflo(q1.y); a1[3] += hw * bfhi(q1.y); a1[4] += hw * bflo(q1.z); a1[5] += hw * bfhi(q1.z); a1[6] += hw * bflo(q1.w); a1[7] += hw * bfhi(q1.w); }
.LBB0_703:
	s_lshl_b32 s5, s1, 13
	s_andn2_b64 vcc, exec, s[2:3]
	s_and_b32 s22, s5, 0x2000
	s_cbranch_vccnz .LBB0_2532
	v_and_b32_e32 v28, 31, v150
	v_and_b32_e32 v16, 3, v150
	v_lshrrev_b32_e32 v0, 1, v150
	v_lshrrev_b32_e32 v1, 3, v150
	s_waitcnt lgkmcnt(0)
	v_and_or_b32 v2, v0, 4, v16
	v_bfe_u32 v0, v28, 2, 1
	v_and_b32_e32 v1, 2, v1
	s_add_i32 s4, s22, s4
	v_or3_b32 v0, v1, v0, s4
	v_mov_b32_e32 v1, v128
	v_lshlrev_b64 v[0:1], 14, v[0:1]
	v_lshrrev_b32_e32 v29, 5, v129
	v_lshl_add_u64 v[0:1], s[74:75], 0, v[0:1]
	v_lshlrev_b32_e32 v2, 6, v2
	v_mov_b32_e32 v3, v128
	v_lshl_add_u64 v[0:1], v[0:1], 0, v[2:3]
	v_lshlrev_b32_e32 v2, 4, v29
	v_lshl_add_u64 v[0:1], v[0:1], 0, v[2:3]
	global_load_dwordx4 v[56:59], v[0:1], off offset:2560
	global_load_dwordx4 v[48:51], v[0:1], off offset:2592
	v_add_co_u32_e32 v0, vcc, s95, v0
	v_lshlrev_b32_e32 v17, 3, v29
	s_nop 0
	v_addc_co_u32_e32 v1, vcc, 0, v1, vcc
	global_load_dwordx4 v[60:63], v[0:1], off offset:2560
	global_load_dwordx4 v[52:55], v[0:1], off offset:2592
	v_or_b32_e32 v0, s4, v29
	v_mov_b32_e32 v1, v128
	v_lshlrev_b64 v[0:1], 14, v[0:1]
	v_lshl_add_u64 v[0:1], s[74:75], 0, v[0:1]
	v_add_co_u32_e32 v2, vcc, 0x8000, v0
	s_nop 0
	v_mov_b32_e32 v68, 0
	v_addc_co_u32_e32 v3, vcc, 0, v1, vcc
	global_load_dwordx4 v[12:15], v[0:1], off offset:2368
	global_load_dwordx4 v[8:11], v[2:3], off offset:2368
	v_add_co_u32_e32 v2, vcc, 0x10000, v0
	v_lshlrev_b32_e32 v24, 1, v17
	s_nop 0
	v_addc_co_u32_e32 v3, vcc, 0, v1, vcc
	v_add_co_u32_e32 v0, vcc, 0x18000, v0
	v_mov_b32_e32 v69, v68
	s_nop 0
	v_addc_co_u32_e32 v1, vcc, 0, v1, vcc
	global_load_dwordx4 v[4:7], v[2:3], off offset:2368
	s_nop 0
	global_load_dwordx4 v[0:3], v[0:1], off offset:2368
	s_lshr_b32 s59, s1, 3
	s_add_i32 s63, s59, 8
	s_lshr_b32 s63, s63, 3
	s_mul_i32 s66, s0, s63
	s_add_i32 s84, s66, s63
	s_add_i32 s59, s59, 1
	s_min_i32 s84, s84, s59
	s_cmp_ge_i32 s66, s84
	s_cbranch_scc1 .Lidx_nopre
	s_lshl_b32 s85, s66, 5
	s_add_i32 s85, s85, s22
	s_sub_i32 s84, s84, 1
	v_or_b32_e32 v228, s85, v28
	v_mov_b32_e32 v229, 0
	v_lshlrev_b64 v[228:229], 6, v[228:229]
	v_mov_b32_e32 v230, v24
	v_mov_b32_e32 v231, 0
	v_lshl_add_u64 v[228:229], s[78:79], 0, v[228:229]
	v_lshl_add_u64 v[228:229], v[228:229], 0, v[230:231]
	s_mov_b32 s87, 0
	global_load_dwordx4 v[188:191], v[228:229], off
	global_load_dwordx4 v[192:195], v[228:229], off offset:32
	s_add_i32 s86, s66, 1
	s_min_i32 s86, s86, s84
	s_sub_i32 s86, s86, s66
	s_lshl_b32 s86, s86, 11
	v_lshl_add_u64 v[232:233], v[228:229], 0, s[86:87]
	global_load_dwordx4 v[196:199], v[232:233], off
	global_load_dwordx4 v[200:203], v[232:233], off offset:32
	s_add_i32 s86, s66, 2
	s_min_i32 s86, s86, s84
	s_sub_i32 s86, s86, s66
	s_lshl_b32 s86, s86, 11
	v_lshl_add_u64 v[232:233], v[228:229], 0, s[86:87]
	global_load_dwordx4 v[204:207], v[232:233], off
	global_load_dwordx4 v[208:211], v[232:233], off offset:32
	s_add_i32 s86, s66, 3
	s_min_i32 s86, s86, s84
	s_sub_i32 s86, s86, s66
	s_lshl_b32 s86, s86, 11
	v_lshl_add_u64 v[232:233], v[228:229], 0, s[86:87]
	global_load_dwordx4 v[220:223], v[232:233], off
	global_load_dwordx4 v[224:227], v[232:233], off offset:32
